# MoE K loop: header last-trip test evaluated before the trip's last barrier on the looping path (on top of v109 rotation)
# baseline (speedup 1.0000x reference)
.LBB0_1441:
	s_addk_i32 s42, 0x100
	s_add_i32 s43, s42, s66
	s_and_b64 s[40:41], s[38:39], exec
	s_waitcnt vmcnt(8)
	s_cselect_b32 s41, s67, s43
	s_add_i32 s42, s42, s57
	s_waitcnt lgkmcnt(0)
	s_and_b64 s[38:39], s[38:39], exec
	s_cselect_b32 s40, s56, s42
	s_add_i32 s38, s41, 0x80
	s_add_i32 s39, s40, 0x80
	s_barrier
	s_setprio 1
	s_waitcnt lgkmcnt(6)
	v_mfma_scale_f32_16x16x128_f8f6f4 v[188:191], v[16:23], v[56:63], v[188:191], v238, v238 op_sel_hi:[0,0,0]
	v_mfma_scale_f32_16x16x128_f8f6f4 v[184:187], v[24:31], v[56:63], v[184:187], v238, v238 op_sel_hi:[0,0,0]
	s_waitcnt lgkmcnt(4)
	v_mfma_scale_f32_16x16x128_f8f6f4 v[180:183], v[16:23], v[48:55], v[180:183], v238, v238 op_sel_hi:[0,0,0]
	v_mfma_scale_f32_16x16x128_f8f6f4 v[176:179], v[24:31], v[48:55], v[176:179], v238, v238 op_sel_hi:[0,0,0]
	s_waitcnt lgkmcnt(2)
	v_mfma_scale_f32_16x16x128_f8f6f4 v[172:175], v[16:23], v[40:47], v[172:175], v238, v238 op_sel_hi:[0,0,0]
	v_mfma_scale_f32_16x16x128_f8f6f4 v[168:171], v[24:31], v[40:47], v[168:171], v238, v238 op_sel_hi:[0,0,0]
	s_waitcnt lgkmcnt(0)
	v_mfma_scale_f32_16x16x128_f8f6f4 v[164:167], v[16:23], v[32:39], v[164:167], v238, v238 op_sel_hi:[0,0,0]
	v_mfma_scale_f32_16x16x128_f8f6f4 v[160:163], v[24:31], v[32:39], v[160:163], v238, v238 op_sel_hi:[0,0,0]
	s_setprio 0
	s_setprio 1
	v_mfma_scale_f32_16x16x128_f8f6f4 v[156:159], v[0:7], v[56:63], v[156:159], v238, v238 op_sel_hi:[0,0,0]
	v_mfma_scale_f32_16x16x128_f8f6f4 v[152:155], v[8:15], v[56:63], v[152:155], v238, v238 op_sel_hi:[0,0,0]
	v_mfma_scale_f32_16x16x128_f8f6f4 v[148:151], v[0:7], v[48:55], v[148:151], v238, v238 op_sel_hi:[0,0,0]
	v_mfma_scale_f32_16x16x128_f8f6f4 v[144:147], v[8:15], v[48:55], v[144:147], v238, v238 op_sel_hi:[0,0,0]
	v_mfma_scale_f32_16x16x128_f8f6f4 v[140:143], v[0:7], v[40:47], v[140:143], v238, v238 op_sel_hi:[0,0,0]
	v_mfma_scale_f32_16x16x128_f8f6f4 v[136:139], v[8:15], v[40:47], v[136:139], v238, v238 op_sel_hi:[0,0,0]
	v_mfma_scale_f32_16x16x128_f8f6f4 v[132:135], v[0:7], v[32:39], v[132:135], v238, v238 op_sel_hi:[0,0,0]
	v_mfma_scale_f32_16x16x128_f8f6f4 v[128:131], v[8:15], v[32:39], v[128:131], v238, v238 op_sel_hi:[0,0,0]
	s_setprio 0
	s_barrier
	s_mov_b32 m0, s74
	s_lshl_b32 s42, s50, 6
	ds_read_b128 v[32:35], v200 offset:16384
	ds_read_b128 v[36:39], v200 offset:17408
	ds_read_b128 v[40:43], v200 offset:18432
	ds_read_b128 v[44:47], v200 offset:19456
	ds_read_b128 v[48:51], v200 offset:20480
	ds_read_b128 v[52:55], v200 offset:21504
	ds_read_b128 v[56:59], v200 offset:22528
	ds_read_b128 v[60:63], v200 offset:23552
	buffer_load_dwordx4 v194, s[60:63], s41 offen lds
	s_add_i32 s41, s42, s41
	s_mov_b32 m0, s75
	s_nop 0
	buffer_load_dwordx4 v194, s[60:63], s41 offen lds
	s_add_i32 s41, s41, s42
	s_mov_b32 m0, s76
	s_nop 0
	buffer_load_dwordx4 v194, s[60:63], s41 offen lds
	s_add_i32 s41, s41, s42
	s_mov_b32 m0, s77
	s_nop 0
	buffer_load_dwordx4 v194, s[60:63], s41 offen lds
	s_mov_b32 m0, s73
	s_nop 0
	buffer_load_dwordx4 v192, s[60:63], s40 offen lds
	s_add_i32 s40, s42, s40
	s_mov_b32 m0, s78
	s_nop 0
	buffer_load_dwordx4 v192, s[60:63], s40 offen lds
	s_waitcnt vmcnt(8)
	s_waitcnt lgkmcnt(0)
	s_barrier
	s_setprio 1
	s_waitcnt lgkmcnt(6)
	v_mfma_scale_f32_16x16x128_f8f6f4 v[124:127], v[16:23], v[32:39], v[124:127], v238, v238 op_sel_hi:[0,0,0]
	v_mfma_scale_f32_16x16x128_f8f6f4 v[120:123], v[24:31], v[32:39], v[120:123], v238, v238 op_sel_hi:[0,0,0]
	s_waitcnt lgkmcnt(4)
	v_mfma_scale_f32_16x16x128_f8f6f4 v[116:119], v[16:23], v[40:47], v[116:119], v238, v238 op_sel_hi:[0,0,0]
	v_mfma_scale_f32_16x16x128_f8f6f4 v[112:115], v[24:31], v[40:47], v[112:115], v238, v238 op_sel_hi:[0,0,0]
	s_waitcnt lgkmcnt(2)
	v_mfma_scale_f32_16x16x128_f8f6f4 v[108:111], v[16:23], v[48:55], v[108:111], v238, v238 op_sel_hi:[0,0,0]
	v_mfma_scale_f32_16x16x128_f8f6f4 v[104:107], v[24:31], v[48:55], v[104:107], v238, v238 op_sel_hi:[0,0,0]
	s_waitcnt lgkmcnt(0)
	v_mfma_scale_f32_16x16x128_f8f6f4 v[100:103], v[16:23], v[56:63], v[100:103], v238, v238 op_sel_hi:[0,0,0]
	v_mfma_scale_f32_16x16x128_f8f6f4 v[96:99], v[24:31], v[56:63], v[96:99], v238, v238 op_sel_hi:[0,0,0]
	s_setprio 0
	s_setprio 1
	v_mfma_scale_f32_16x16x128_f8f6f4 v[92:95], v[0:7], v[32:39], v[92:95], v238, v238 op_sel_hi:[0,0,0]
	v_mfma_scale_f32_16x16x128_f8f6f4 v[88:91], v[8:15], v[32:39], v[88:91], v238, v238 op_sel_hi:[0,0,0]
	v_mfma_scale_f32_16x16x128_f8f6f4 v[84:87], v[0:7], v[40:47], v[84:87], v238, v238 op_sel_hi:[0,0,0]
	v_mfma_scale_f32_16x16x128_f8f6f4 v[80:83], v[8:15], v[40:47], v[80:83], v238, v238 op_sel_hi:[0,0,0]
	v_mfma_scale_f32_16x16x128_f8f6f4 v[76:79], v[0:7], v[48:55], v[76:79], v238, v238 op_sel_hi:[0,0,0]
	v_mfma_scale_f32_16x16x128_f8f6f4 v[72:75], v[8:15], v[48:55], v[72:75], v238, v238 op_sel_hi:[0,0,0]
	v_mfma_scale_f32_16x16x128_f8f6f4 v[68:71], v[0:7], v[56:63], v[68:71], v238, v238 op_sel_hi:[0,0,0]
	v_mfma_scale_f32_16x16x128_f8f6f4 v[64:67], v[8:15], v[56:63], v[64:67], v238, v238 op_sel_hi:[0,0,0]
	s_setprio 0
	s_barrier
	ds_read_b128 v[0:3], v199 offset:32768
	ds_read_b128 v[4:7], v199 offset:33792
	ds_read_b128 v[8:11], v199 offset:34816
	ds_read_b128 v[12:15], v199 offset:35840
	ds_read_b128 v[16:19], v199 offset:49152
	ds_read_b128 v[20:23], v199 offset:50176
	ds_read_b128 v[24:27], v199 offset:51200
	ds_read_b128 v[28:31], v199 offset:52224
	s_mov_b32 m0, s79
	s_add_i32 s40, s40, s42
	ds_read_b128 v[32:35], v200 offset:32768
	ds_read_b128 v[36:39], v200 offset:33792
	ds_read_b128 v[40:43], v200 offset:34816
	ds_read_b128 v[44:47], v200 offset:35840
	ds_read_b128 v[48:51], v200 offset:36864
	ds_read_b128 v[52:55], v200 offset:37888
	ds_read_b128 v[56:59], v200 offset:38912
	ds_read_b128 v[60:63], v200 offset:39936
	buffer_load_dwordx4 v192, s[60:63], s40 offen lds
	s_add_i32 s40, s40, s42
	s_mov_b32 m0, s80
	s_nop 0
	buffer_load_dwordx4 v192, s[60:63], s40 offen lds
	s_waitcnt vmcnt(8)
	s_waitcnt lgkmcnt(0)
	s_barrier
	s_setprio 1
	s_waitcnt lgkmcnt(6)
	v_mfma_scale_f32_16x16x128_f8f6f4 v[188:191], v[0:7], v[32:39], v[188:191], v238, v238 op_sel_hi:[0,0,0]
	v_mfma_scale_f32_16x16x128_f8f6f4 v[184:187], v[8:15], v[32:39], v[184:187], v238, v238 op_sel_hi:[0,0,0]
	s_waitcnt lgkmcnt(4)
	v_mfma_scale_f32_16x16x128_f8f6f4 v[180:183], v[0:7], v[40:47], v[180:183], v238, v238 op_sel_hi:[0,0,0]
	v_mfma_scale_f32_16x16x128_f8f6f4 v[176:179], v[8:15], v[40:47], v[176:179], v238, v238 op_sel_hi:[0,0,0]
	s_waitcnt lgkmcnt(2)
	v_mfma_scale_f32_16x16x128_f8f6f4 v[172:175], v[0:7], v[48:55], v[172:175], v238, v238 op_sel_hi:[0,0,0]
	v_mfma_scale_f32_16x16x128_f8f6f4 v[168:171], v[8:15], v[48:55], v[168:171], v238, v238 op_sel_hi:[0,0,0]
	s_waitcnt lgkmcnt(0)
	v_mfma_scale_f32_16x16x128_f8f6f4 v[164:167], v[0:7], v[56:63], v[164:167], v238, v238 op_sel_hi:[0,0,0]
	v_mfma_scale_f32_16x16x128_f8f6f4 v[160:163], v[8:15], v[56:63], v[160:163], v238, v238 op_sel_hi:[0,0,0]
	s_setprio 0
	s_setprio 1
	v_mfma_scale_f32_16x16x128_f8f6f4 v[156:159], v[16:23], v[32:39], v[156:159], v238, v238 op_sel_hi:[0,0,0]
	v_mfma_scale_f32_16x16x128_f8f6f4 v[152:155], v[24:31], v[32:39], v[152:155], v238, v238 op_sel_hi:[0,0,0]
	v_mfma_scale_f32_16x16x128_f8f6f4 v[148:151], v[16:23], v[40:47], v[148:151], v238, v238 op_sel_hi:[0,0,0]
	v_mfma_scale_f32_16x16x128_f8f6f4 v[144:147], v[24:31], v[40:47], v[144:147], v238, v238 op_sel_hi:[0,0,0]
	v_mfma_scale_f32_16x16x128_f8f6f4 v[140:143], v[16:23], v[48:55], v[140:143], v238, v238 op_sel_hi:[0,0,0]
	v_mfma_scale_f32_16x16x128_f8f6f4 v[136:139], v[24:31], v[48:55], v[136:139], v238, v238 op_sel_hi:[0,0,0]
	v_mfma_scale_f32_16x16x128_f8f6f4 v[132:135], v[16:23], v[56:63], v[132:135], v238, v238 op_sel_hi:[0,0,0]
	v_mfma_scale_f32_16x16x128_f8f6f4 v[128:131], v[24:31], v[56:63], v[128:131], v238, v238 op_sel_hi:[0,0,0]
	s_setprio 0
	s_barrier
	s_mov_b32 m0, s83
	ds_read_b128 v[32:35], v200 offset:49152
	ds_read_b128 v[36:39], v200 offset:50176
	ds_read_b128 v[40:43], v200 offset:51200
	ds_read_b128 v[44:47], v200 offset:52224
	ds_read_b128 v[48:51], v200 offset:53248
	ds_read_b128 v[52:55], v200 offset:54272
	ds_read_b128 v[56:59], v200 offset:55296
	ds_read_b128 v[60:63], v200 offset:56320
	buffer_load_dwordx4 v194, s[60:63], s38 offen lds
	s_add_i32 s38, s42, s38
	s_mov_b32 m0, s84
	s_nop 0
	buffer_load_dwordx4 v194, s[60:63], s38 offen lds
	s_add_i32 s38, s38, s42
	s_mov_b32 m0, s87
	s_nop 0
	buffer_load_dwordx4 v194, s[60:63], s38 offen lds
	s_add_i32 s38, s38, s42
	s_mov_b32 m0, s90
	s_add_i32 s42, s42, s39
	buffer_load_dwordx4 v194, s[60:63], s38 offen lds
	s_mov_b32 m0, s85
	s_nop 0
	buffer_load_dwordx4 v192, s[60:63], s39 offen lds
	s_mov_b32 m0, s86
	s_nop 0
	buffer_load_dwordx4 v192, s[60:63], s42 offen lds
	s_waitcnt vmcnt(8)
	s_waitcnt lgkmcnt(0)
	s_barrier
	s_setprio 1
	s_waitcnt lgkmcnt(6)
	v_mfma_scale_f32_16x16x128_f8f6f4 v[124:127], v[0:7], v[32:39], v[124:127], v238, v238 op_sel_hi:[0,0,0]
	v_mfma_scale_f32_16x16x128_f8f6f4 v[120:123], v[8:15], v[32:39], v[120:123], v238, v238 op_sel_hi:[0,0,0]
	s_waitcnt lgkmcnt(4)
	v_mfma_scale_f32_16x16x128_f8f6f4 v[116:119], v[0:7], v[40:47], v[116:119], v238, v238 op_sel_hi:[0,0,0]
	v_mfma_scale_f32_16x16x128_f8f6f4 v[112:115], v[8:15], v[40:47], v[112:115], v238, v238 op_sel_hi:[0,0,0]
	s_waitcnt lgkmcnt(2)
	v_mfma_scale_f32_16x16x128_f8f6f4 v[108:111], v[0:7], v[48:55], v[108:111], v238, v238 op_sel_hi:[0,0,0]
	v_mfma_scale_f32_16x16x128_f8f6f4 v[104:107], v[8:15], v[48:55], v[104:107], v238, v238 op_sel_hi:[0,0,0]
	s_waitcnt lgkmcnt(0)
	v_mfma_scale_f32_16x16x128_f8f6f4 v[100:103], v[0:7], v[56:63], v[100:103], v238, v238 op_sel_hi:[0,0,0]
	v_mfma_scale_f32_16x16x128_f8f6f4 v[96:99], v[8:15], v[56:63], v[96:99], v238, v238 op_sel_hi:[0,0,0]
	s_setprio 0
	s_setprio 1
	v_mfma_scale_f32_16x16x128_f8f6f4 v[92:95], v[16:23], v[32:39], v[92:95], v238, v238 op_sel_hi:[0,0,0]
	v_mfma_scale_f32_16x16x128_f8f6f4 v[88:91], v[24:31], v[32:39], v[88:91], v238, v238 op_sel_hi:[0,0,0]
	v_mfma_scale_f32_16x16x128_f8f6f4 v[84:87], v[16:23], v[40:47], v[84:87], v238, v238 op_sel_hi:[0,0,0]
	v_mfma_scale_f32_16x16x128_f8f6f4 v[80:83], v[24:31], v[40:47], v[80:83], v238, v238 op_sel_hi:[0,0,0]
	v_mfma_scale_f32_16x16x128_f8f6f4 v[76:79], v[16:23], v[48:55], v[76:79], v238, v238 op_sel_hi:[0,0,0]
	v_mfma_scale_f32_16x16x128_f8f6f4 v[72:75], v[24:31], v[48:55], v[72:75], v238, v238 op_sel_hi:[0,0,0]
	v_mfma_scale_f32_16x16x128_f8f6f4 v[68:71], v[16:23], v[56:63], v[68:71], v238, v238 op_sel_hi:[0,0,0]
	v_mfma_scale_f32_16x16x128_f8f6f4 v[64:67], v[24:31], v[56:63], v[64:67], v238, v238 op_sel_hi:[0,0,0]
	s_add_i32 s82, s82, 2
	s_cmp_eq_u32 s82, s22
	s_cselect_b64 s[38:39], -1, 0
	s_and_b64 s[40:41], s[14:15], s[38:39]
	s_and_b64 s[42:43], s[6:7], s[40:41]
	s_andn2_b64 vcc, exec, s[42:43]
	s_cmp_ge_u32 s82, s96
	s_setprio 0
	s_barrier
	s_cbranch_scc1 .LBB0_1464
	s_cbranch_vccnz .LBB0_1462
	s_branch .Lmoe_hdr_after

.Lmoe_hdr_after:
	s_cmp_lt_i32 s64, 0
	s_cbranch_scc1 .LBB0_1447
	s_waitcnt vmcnt(0)
	s_and_saveexec_b64 s[42:43], s[2:3]
	s_cbranch_execz .LBB0_1446
	s_lshl_b32 s64, s64, 6
	s_lshl_b64 s[44:45], s[64:65], 2
	s_add_u32 s44, s58, s44
	s_addc_u32 s45, s59, s45
	global_atomic_add v209, v211, s[44:45]
